# f5
# speedup vs baseline: 1.0549x; 1.0054x over previous
_Z14special_kernelPKtPKfS2_S2_S2_PfS3_S3_S2_S3_:
	s_load_dwordx2 s[16:17], s[0:1], 0x40
	s_load_dwordx4 s[8:11], s[0:1], 0x8
	s_load_dwordx2 s[6:7], s[0:1], 0x18
	v_lshrrev_b32_e32 v1, 8, v0
	v_lshlrev_b32_e32 v22, 6, v1
	s_cmp_lg_u32 s2, 32
	s_mov_b64 s[4:5], -1
	s_cbranch_scc0 .LBB12_12
	s_load_dwordx4 s[12:15], s[0:1], 0x20
	s_load_dwordx2 s[18:19], s[0:1], 0x30
	v_mov_b32_e32 v2, 2
	v_lshlrev_b32_sdwa v2, v2, v0 dst_sel:DWORD dst_unused:UNUSED_PAD src0_sel:DWORD src1_sel:BYTE_0
	v_lshl_or_b32 v16, v1, 16, v2
	v_mov_b32_e32 v3, 0
	v_lshlrev_b32_e32 v24, 8, v1
	v_add_u32_e32 v23, 64, v22
	v_or_b32_e32 v2, 0x3c00, v16
	v_or_b32_e32 v4, 0x3400, v16
	v_mov_b32_e32 v5, v3
	v_or_b32_e32 v25, 0x2000, v24
	v_or_b32_e32 v6, 0x2c00, v16
	v_mov_b32_e32 v7, v3
	v_or_b32_e32 v8, 0x400, v16
	v_mov_b32_e32 v9, v3
	v_or_b32_e32 v10, 0x2400, v16
	v_mov_b32_e32 v11, v3
	v_or_b32_e32 v12, 0x1c00, v16
	v_mov_b32_e32 v13, v3
	v_or_b32_e32 v14, 0xc00, v16
	v_mov_b32_e32 v15, v3
	v_or_b32_e32 v16, 0x1400, v16
	v_mov_b32_e32 v17, v3
	s_mov_b64 s[4:5], 0
	s_waitcnt lgkmcnt(0)
	s_mov_b64 s[20:21], s[8:9]
	v_mov_b32_e32 v26, v22
	v_mov_b32_e32 v18, v3
	v_mov_b32_e32 v19, v3
	v_mov_b32_e32 v20, v3
	v_mov_b32_e32 v21, v3
	v_lshl_add_u64 v[28:29], s[20:21], 0, v[8:9]
	v_lshl_add_u64 v[30:31], s[20:21], 0, v[14:15]
	v_lshl_add_u64 v[32:33], s[20:21], 0, v[16:17]
	v_lshl_add_u64 v[34:35], s[20:21], 0, v[12:13]
	v_lshl_add_u64 v[36:37], s[20:21], 0, v[10:11]
	v_lshl_add_u64 v[38:39], s[20:21], 0, v[6:7]
	v_lshl_add_u64 v[40:41], s[20:21], 0, v[4:5]
	v_lshl_add_u64 v[42:43], s[20:21], 0, v[2:3]
	global_load_dword v56, v[28:29], off offset:-1024
	global_load_dword v57, v[28:29], off
	global_load_dword v58, v[30:31], off offset:-1024
	global_load_dword v59, v[30:31], off
	global_load_dword v60, v[32:33], off offset:-1024
	global_load_dword v61, v[32:33], off
	global_load_dword v62, v[34:35], off offset:-1024
	global_load_dword v63, v[34:35], off
	global_load_dword v64, v[36:37], off offset:-1024
	global_load_dword v65, v[36:37], off
	global_load_dword v66, v[38:39], off offset:-1024
	global_load_dword v67, v[38:39], off
	global_load_dword v68, v[40:41], off offset:-1024
	global_load_dword v69, v[40:41], off
	global_load_dword v70, v[42:43], off offset:-1024
	global_load_dword v71, v[42:43], off
	s_add_u32 s20, s20, 0x4000
	s_addc_u32 s21, s21, 0
	v_lshl_add_u64 v[28:29], s[20:21], 0, v[8:9]
	v_lshl_add_u64 v[30:31], s[20:21], 0, v[14:15]
	v_lshl_add_u64 v[32:33], s[20:21], 0, v[16:17]
	v_lshl_add_u64 v[34:35], s[20:21], 0, v[12:13]
	v_lshl_add_u64 v[36:37], s[20:21], 0, v[10:11]
	v_lshl_add_u64 v[38:39], s[20:21], 0, v[6:7]
	v_lshl_add_u64 v[40:41], s[20:21], 0, v[4:5]
	v_lshl_add_u64 v[42:43], s[20:21], 0, v[2:3]
	global_load_dword v72, v[28:29], off offset:-1024
	global_load_dword v73, v[28:29], off
	global_load_dword v74, v[30:31], off offset:-1024
	global_load_dword v75, v[30:31], off
	global_load_dword v76, v[32:33], off offset:-1024
	global_load_dword v77, v[32:33], off
	global_load_dword v78, v[34:35], off offset:-1024
	global_load_dword v79, v[34:35], off
	global_load_dword v80, v[36:37], off offset:-1024
	global_load_dword v81, v[36:37], off
	global_load_dword v82, v[38:39], off offset:-1024
	global_load_dword v83, v[38:39], off
	global_load_dword v84, v[40:41], off offset:-1024
	global_load_dword v85, v[40:41], off
	global_load_dword v86, v[42:43], off offset:-1024
	global_load_dword v87, v[42:43], off
	s_add_u32 s20, s20, 0x4000
	s_addc_u32 s21, s21, 0
	v_lshl_add_u64 v[28:29], s[20:21], 0, v[8:9]
	v_lshl_add_u64 v[30:31], s[20:21], 0, v[14:15]
	v_lshl_add_u64 v[32:33], s[20:21], 0, v[16:17]
	v_lshl_add_u64 v[34:35], s[20:21], 0, v[12:13]
	v_lshl_add_u64 v[36:37], s[20:21], 0, v[10:11]
	v_lshl_add_u64 v[38:39], s[20:21], 0, v[6:7]
	v_lshl_add_u64 v[40:41], s[20:21], 0, v[4:5]
	v_lshl_add_u64 v[42:43], s[20:21], 0, v[2:3]
	global_load_dword v88, v[28:29], off offset:-1024
	global_load_dword v89, v[28:29], off
	global_load_dword v90, v[30:31], off offset:-1024
	global_load_dword v91, v[30:31], off
	global_load_dword v92, v[32:33], off offset:-1024
	global_load_dword v93, v[32:33], off
	global_load_dword v94, v[34:35], off offset:-1024
	global_load_dword v95, v[34:35], off
	global_load_dword v96, v[36:37], off offset:-1024
	global_load_dword v97, v[36:37], off
	global_load_dword v98, v[38:39], off offset:-1024
	global_load_dword v99, v[38:39], off
	global_load_dword v100, v[40:41], off offset:-1024
	global_load_dword v101, v[40:41], off
	global_load_dword v102, v[42:43], off offset:-1024
	global_load_dword v103, v[42:43], off
	s_add_u32 s20, s20, 0x4000
	s_addc_u32 s21, s21, 0
	s_movk_i32 s3, 0x200
	v_cmp_gt_u32_e32 vcc, s3, v0
	s_and_saveexec_b64 s[4:5], vcc
	s_cbranch_execz .LBB12_3
	s_load_dwordx2 s[24:25], s[0:1], 0x0
	s_mul_i32 s26, s2, 0x210
	v_lshrrev_b32_e32 v124, 4, v0
	s_mul_hi_i32 s3, s2, 0x210
	s_add_u32 s26, s26, 0x200
	v_bfe_u32 v125, v0, 4, 1
	s_addc_u32 s3, s3, 0
	v_and_b32_e32 v124, 14, v124
	v_lshrrev_b32_e32 v126, 1, v0
	v_and_b32_e32 v127, 3, v0
	v_or3_b32 v124, s26, v124, v125
	v_mov_b32_e32 v125, s3
	v_and_or_b32 v122, v126, 4, v127
	v_lshlrev_b64 v[124:125], 10, v[124:125]
	v_lshlrev_b32_e32 v126, 7, v0
	s_waitcnt lgkmcnt(0)
	v_lshl_add_u64 v[124:125], s[24:25], 0, v[124:125]
	v_and_b32_e32 v126, 0x200, v126
	v_mov_b32_e32 v127, 0
	v_lshl_add_u64 v[124:125], v[124:125], 0, v[126:127]
	v_lshlrev_b32_e32 v126, 4, v1
	v_lshl_add_u64 v[124:125], v[124:125], 0, v[126:127]
	v_lshlrev_b32_e32 v126, 1, v122
	v_lshl_add_u64 v[124:125], v[124:125], 0, v[126:127]
	global_load_ushort v124, v[124:125], off
	v_mov_b32_e32 v125, 2
	v_lshlrev_b32_sdwa v125, v125, v0 dst_sel:DWORD dst_unused:UNUSED_PAD src0_sel:DWORD src1_sel:BYTE_0
	global_load_dword v126, v125, s[16:17]
	v_lshl_or_b32 v125, v1, 10, v125
	s_waitcnt vmcnt(1)
	v_lshlrev_b32_e32 v124, 16, v124
	s_waitcnt vmcnt(0)
	v_add_f32_e32 v124, v126, v124
	ds_write_b32 v125, v124 offset:8192
.LBB12_3:
	s_or_b64 exec, exec, s[4:5]
	s_waitcnt lgkmcnt(0)
	s_barrier
	ds_read_b128 v[28:31], v25 offset:0
	ds_read_b128 v[32:35], v25 offset:16
	ds_read_b128 v[36:39], v25 offset:32
	ds_read_b128 v[40:43], v25 offset:48
	ds_read_b128 v[44:47], v25 offset:1024
	ds_read_b128 v[48:51], v25 offset:1040
	ds_read_b128 v[52:55], v25 offset:1056
	ds_read_b128 v[120:123], v25 offset:1072
	s_waitcnt vmcnt(32) lgkmcnt(0)
	v_pk_fma_f32 v[20:21], v[56:57], v[28:29], v[20:21]
	v_pk_fma_f32 v[18:19], v[56:57], v[44:45], v[18:19]
	v_pk_fma_f32 v[20:21], v[58:59], v[30:31], v[20:21]
	v_pk_fma_f32 v[18:19], v[58:59], v[46:47], v[18:19]
	v_pk_fma_f32 v[20:21], v[60:61], v[32:33], v[20:21]
	v_pk_fma_f32 v[18:19], v[60:61], v[48:49], v[18:19]
	v_pk_fma_f32 v[20:21], v[62:63], v[34:35], v[20:21]
	v_pk_fma_f32 v[18:19], v[62:63], v[50:51], v[18:19]
	v_pk_fma_f32 v[20:21], v[64:65], v[36:37], v[20:21]
	v_pk_fma_f32 v[18:19], v[64:65], v[52:53], v[18:19]
	v_pk_fma_f32 v[20:21], v[66:67], v[38:39], v[20:21]
	v_pk_fma_f32 v[18:19], v[66:67], v[54:55], v[18:19]
	v_pk_fma_f32 v[20:21], v[68:69], v[40:41], v[20:21]
	v_pk_fma_f32 v[18:19], v[68:69], v[120:121], v[18:19]
	v_pk_fma_f32 v[20:21], v[70:71], v[42:43], v[20:21]
	v_pk_fma_f32 v[18:19], v[70:71], v[122:123], v[18:19]
	v_lshl_add_u64 v[28:29], s[20:21], 0, v[8:9]
	v_lshl_add_u64 v[30:31], s[20:21], 0, v[14:15]
	v_lshl_add_u64 v[32:33], s[20:21], 0, v[16:17]
	v_lshl_add_u64 v[34:35], s[20:21], 0, v[12:13]
	v_lshl_add_u64 v[36:37], s[20:21], 0, v[10:11]
	v_lshl_add_u64 v[38:39], s[20:21], 0, v[6:7]
	v_lshl_add_u64 v[40:41], s[20:21], 0, v[4:5]
	v_lshl_add_u64 v[42:43], s[20:21], 0, v[2:3]
	global_load_dword v104, v[28:29], off offset:-1024
	global_load_dword v105, v[28:29], off
	global_load_dword v106, v[30:31], off offset:-1024
	global_load_dword v107, v[30:31], off
	global_load_dword v108, v[32:33], off offset:-1024
	global_load_dword v109, v[32:33], off
	global_load_dword v110, v[34:35], off offset:-1024
	global_load_dword v111, v[34:35], off
	global_load_dword v112, v[36:37], off offset:-1024
	global_load_dword v113, v[36:37], off
	global_load_dword v114, v[38:39], off offset:-1024
	global_load_dword v115, v[38:39], off
	global_load_dword v116, v[40:41], off offset:-1024
	global_load_dword v117, v[40:41], off
	global_load_dword v118, v[42:43], off offset:-1024
	global_load_dword v119, v[42:43], off
	s_add_u32 s20, s20, 0x4000
	s_addc_u32 s21, s21, 0
	ds_read_b128 v[28:31], v25 offset:64
	ds_read_b128 v[32:35], v25 offset:80
	ds_read_b128 v[36:39], v25 offset:96
	ds_read_b128 v[40:43], v25 offset:112
	ds_read_b128 v[44:47], v25 offset:1088
	ds_read_b128 v[48:51], v25 offset:1104
	ds_read_b128 v[52:55], v25 offset:1120
	ds_read_b128 v[120:123], v25 offset:1136
	s_waitcnt vmcnt(32) lgkmcnt(0)
	v_pk_fma_f32 v[20:21], v[72:73], v[28:29], v[20:21]
	v_pk_fma_f32 v[18:19], v[72:73], v[44:45], v[18:19]
	v_pk_fma_f32 v[20:21], v[74:75], v[30:31], v[20:21]
	v_pk_fma_f32 v[18:19], v[74:75], v[46:47], v[18:19]
	v_pk_fma_f32 v[20:21], v[76:77], v[32:33], v[20:21]
	v_pk_fma_f32 v[18:19], v[76:77], v[48:49], v[18:19]
	v_pk_fma_f32 v[20:21], v[78:79], v[34:35], v[20:21]
	v_pk_fma_f32 v[18:19], v[78:79], v[50:51], v[18:19]
	v_pk_fma_f32 v[20:21], v[80:81], v[36:37], v[20:21]
	v_pk_fma_f32 v[18:19], v[80:81], v[52:53], v[18:19]
	v_pk_fma_f32 v[20:21], v[82:83], v[38:39], v[20:21]
	v_pk_fma_f32 v[18:19], v[82:83], v[54:55], v[18:19]
	v_pk_fma_f32 v[20:21], v[84:85], v[40:41], v[20:21]
	v_pk_fma_f32 v[18:19], v[84:85], v[120:121], v[18:19]
	v_pk_fma_f32 v[20:21], v[86:87], v[42:43], v[20:21]
	v_pk_fma_f32 v[18:19], v[86:87], v[122:123], v[18:19]
	ds_read_b128 v[28:31], v25 offset:128
	ds_read_b128 v[32:35], v25 offset:144
	ds_read_b128 v[36:39], v25 offset:160
	ds_read_b128 v[40:43], v25 offset:176
	ds_read_b128 v[44:47], v25 offset:1152
	ds_read_b128 v[48:51], v25 offset:1168
	ds_read_b128 v[52:55], v25 offset:1184
	ds_read_b128 v[120:123], v25 offset:1200
	s_waitcnt vmcnt(16) lgkmcnt(0)
	v_pk_fma_f32 v[20:21], v[88:89], v[28:29], v[20:21]
	v_pk_fma_f32 v[18:19], v[88:89], v[44:45], v[18:19]
	v_pk_fma_f32 v[20:21], v[90:91], v[30:31], v[20:21]
	v_pk_fma_f32 v[18:19], v[90:91], v[46:47], v[18:19]
	v_pk_fma_f32 v[20:21], v[92:93], v[32:33], v[20:21]
	v_pk_fma_f32 v[18:19], v[92:93], v[48:49], v[18:19]
	v_pk_fma_f32 v[20:21], v[94:95], v[34:35], v[20:21]
	v_pk_fma_f32 v[18:19], v[94:95], v[50:51], v[18:19]
	v_pk_fma_f32 v[20:21], v[96:97], v[36:37], v[20:21]
	v_pk_fma_f32 v[18:19], v[96:97], v[52:53], v[18:19]
	v_pk_fma_f32 v[20:21], v[98:99], v[38:39], v[20:21]
	v_pk_fma_f32 v[18:19], v[98:99], v[54:55], v[18:19]
	v_pk_fma_f32 v[20:21], v[100:101], v[40:41], v[20:21]
	v_pk_fma_f32 v[18:19], v[100:101], v[120:121], v[18:19]
	v_pk_fma_f32 v[20:21], v[102:103], v[42:43], v[20:21]
	v_pk_fma_f32 v[18:19], v[102:103], v[122:123], v[18:19]
	ds_read_b128 v[28:31], v25 offset:192
	ds_read_b128 v[32:35], v25 offset:208
	ds_read_b128 v[36:39], v25 offset:224
	ds_read_b128 v[40:43], v25 offset:240
	ds_read_b128 v[44:47], v25 offset:1216
	ds_read_b128 v[48:51], v25 offset:1232
	ds_read_b128 v[52:55], v25 offset:1248
	ds_read_b128 v[120:123], v25 offset:1264
	s_waitcnt vmcnt(0) lgkmcnt(0)
	v_pk_fma_f32 v[20:21], v[104:105], v[28:29], v[20:21]
	v_pk_fma_f32 v[18:19], v[104:105], v[44:45], v[18:19]
	v_pk_fma_f32 v[20:21], v[106:107], v[30:31], v[20:21]
	v_pk_fma_f32 v[18:19], v[106:107], v[46:47], v[18:19]
	v_pk_fma_f32 v[20:21], v[108:109], v[32:33], v[20:21]
	v_pk_fma_f32 v[18:19], v[108:109], v[48:49], v[18:19]
	v_pk_fma_f32 v[20:21], v[110:111], v[34:35], v[20:21]
	v_pk_fma_f32 v[18:19], v[110:111], v[50:51], v[18:19]
	v_pk_fma_f32 v[20:21], v[112:113], v[36:37], v[20:21]
	v_pk_fma_f32 v[18:19], v[112:113], v[52:53], v[18:19]
	v_pk_fma_f32 v[20:21], v[114:115], v[38:39], v[20:21]
	v_pk_fma_f32 v[18:19], v[114:115], v[54:55], v[18:19]
	v_pk_fma_f32 v[20:21], v[116:117], v[40:41], v[20:21]
	v_pk_fma_f32 v[18:19], v[116:117], v[120:121], v[18:19]
	v_pk_fma_f32 v[20:21], v[118:119], v[42:43], v[20:21]
	v_pk_fma_f32 v[18:19], v[118:119], v[122:123], v[18:19]
	s_or_b64 exec, exec, s[4:5]
	v_add_f32_e32 v20, v20, v21
	v_mov_b32_e32 v21, 2
	v_lshlrev_b32_sdwa v26, v21, v0 dst_sel:DWORD dst_unused:UNUSED_PAD src0_sel:DWORD src1_sel:BYTE_0
	v_lshl_or_b32 v25, v1, 10, v26
	v_add_f32_e32 v18, v18, v19
	s_movk_i32 s3, 0x100
	ds_write2st64_b32 v25, v20, v18 offset1:16
	v_cmp_gt_u32_e64 s[4:5], s3, v0
	v_lshl_or_b32 v18, s2, 8, v0
	s_waitcnt lgkmcnt(0)
	s_barrier
	s_and_saveexec_b64 s[20:21], s[4:5]
	s_cbranch_execz .LBB12_7
	v_lshl_or_b32 v20, s2, 11, v0
	s_lshl_b32 s2, s2, 13
	s_and_b32 s2, s2, 0xe000
	v_lshl_or_b32 v28, v0, 2, s2
	v_mov_b32_e32 v29, 0
	s_movk_i32 s3, 0x1000
	v_lshl_add_u64 v[30:31], s[12:13], 0, v[28:29]
	v_add_co_u32_e32 v32, vcc, s3, v30
	s_mov_b32 s2, 0x10000
	s_nop 0
	v_addc_co_u32_e32 v33, vcc, 0, v31, vcc
	v_add_co_u32_e32 v34, vcc, s2, v30
	s_mov_b32 s2, 0x11000
	s_nop 0
	v_addc_co_u32_e32 v35, vcc, 0, v31, vcc
	v_add_co_u32_e32 v36, vcc, s2, v30
	s_mov_b32 s2, 0x20000
	s_nop 0
	v_addc_co_u32_e32 v37, vcc, 0, v31, vcc
	v_add_co_u32_e32 v38, vcc, s2, v30
	v_ashrrev_i32_e32 v21, 31, v20
	s_nop 0
	v_addc_co_u32_e32 v39, vcc, 0, v31, vcc
	s_mov_b32 s2, 0x21000
	v_lshl_add_u64 v[20:21], v[20:21], 2, s[12:13]
	v_add_co_u32_e32 v40, vcc, s2, v30
	global_load_dword v19, v[20:21], off
	global_load_dword v27, v[20:21], off offset:1024
	v_addc_co_u32_e32 v41, vcc, 0, v31, vcc
	global_load_dword v42, v[32:33], off
	global_load_dword v43, v[32:33], off offset:1024
	global_load_dword v44, v[32:33], off offset:2048
	global_load_dword v45, v[32:33], off offset:3072
	global_load_dword v46, v[34:35], off offset:1024
	global_load_dword v47, v[34:35], off offset:2048
	global_load_dword v48, v[34:35], off offset:3072
	global_load_dword v49, v[38:39], off offset:1024
	global_load_dword v50, v28, s[12:13]
	global_load_dword v51, v28, s[12:13] offset:1024
	global_load_dword v52, v28, s[12:13] offset:2048
	global_load_dword v53, v[38:39], off offset:2048
	global_load_dword v54, v[38:39], off offset:3072
	global_load_dword v55, v28, s[12:13] offset:3072
	global_load_dword v56, v[36:37], off offset:-4096
	global_load_dword v33, v[36:37], off
	global_load_dword v35, v[36:37], off offset:1024
	s_nop 0
	global_load_dword v38, v[36:37], off offset:2048
	global_load_dword v39, v[36:37], off offset:3072
	global_load_dword v57, v[40:41], off offset:-4096
	global_load_dword v58, v[40:41], off
	s_mov_b32 s2, 0x30000
	v_add_co_u32_e32 v28, vcc, s2, v30
	s_mov_b32 s2, 0x31000
	s_nop 0
	v_addc_co_u32_e32 v29, vcc, 0, v31, vcc
	v_add_co_u32_e32 v30, vcc, s2, v30
	s_waitcnt vmcnt(22)
	v_add_f32_e32 v19, 0, v19
	v_addc_co_u32_e32 v31, vcc, 0, v31, vcc
	global_load_dword v37, v[40:41], off offset:1024
	global_load_dword v59, v[40:41], off offset:2048
	global_load_dword v60, v[40:41], off offset:3072
	global_load_dword v61, v[30:31], off offset:-4096
	global_load_dword v62, v[28:29], off offset:1024
	global_load_dword v63, v[28:29], off offset:2048
	global_load_dword v64, v[28:29], off offset:3072
	global_load_dword v65, v[30:31], off
	v_add_co_u32_e32 v28, vcc, 0x1000, v20
	s_waitcnt vmcnt(29)
	v_add_f32_e32 v19, v19, v27
	v_addc_co_u32_e32 v29, vcc, 0, v21, vcc
	global_load_dword v66, v[20:21], off offset:2048
	global_load_dword v67, v[20:21], off offset:3072
	global_load_dword v68, v[28:29], off
	s_nop 0
	global_load_dword v20, v[28:29], off offset:1024
	global_load_dword v32, v[28:29], off offset:2048
	s_nop 0
	global_load_dword v28, v[28:29], off offset:3072
	s_nop 0
	global_load_dword v29, v26, s[6:7]
	global_load_dword v34, v[30:31], off offset:1024
	global_load_dword v36, v[30:31], off offset:2048
	s_nop 0
	global_load_dword v30, v[30:31], off offset:3072
	s_waitcnt vmcnt(30)
	v_add_f32_e32 v21, 0, v50
	s_waitcnt vmcnt(29)
	v_add_f32_e32 v21, v21, v51
	s_waitcnt vmcnt(28)
	v_add_f32_e32 v21, v21, v52
	s_waitcnt vmcnt(25)
	v_add_f32_e32 v21, v21, v55
	v_add_f32_e32 v21, v21, v42
	v_add_f32_e32 v21, v21, v43
	v_add_f32_e32 v21, v21, v44
	v_add_f32_e32 v21, v21, v45
	s_waitcnt vmcnt(24)
	v_add_f32_e32 v21, v21, v56
	v_add_f32_e32 v21, v21, v46
	v_add_f32_e32 v21, v21, v47
	v_add_f32_e32 v21, v21, v48
	s_waitcnt vmcnt(23)
	v_add_f32_e32 v21, v21, v33
	s_waitcnt vmcnt(22)
	v_add_f32_e32 v21, v21, v35
	s_waitcnt vmcnt(21)
	v_add_f32_e32 v21, v21, v38
	s_waitcnt vmcnt(20)
	v_add_f32_e32 v21, v21, v39
	s_waitcnt vmcnt(19)
	v_add_f32_e32 v21, v21, v57
	v_add_f32_e32 v21, v21, v49
	v_add_f32_e32 v21, v21, v53
	v_add_f32_e32 v21, v21, v54
	s_waitcnt vmcnt(18)
	v_add_f32_e32 v21, v21, v58
	ds_read2st64_b32 v[40:41], v26 offset0:8 offset1:12
	ds_read2st64_b32 v[42:43], v26 offset1:4
	s_waitcnt lgkmcnt(1)
	v_add_f32_e32 v33, v40, v41
	s_waitcnt lgkmcnt(0)
	v_mov_b32_e32 v45, v42
	s_waitcnt vmcnt(17)
	v_add_f32_e32 v21, v21, v37
	s_waitcnt vmcnt(16)
	v_add_f32_e32 v21, v21, v59
	s_waitcnt vmcnt(15)
	v_add_f32_e32 v21, v21, v60
	s_waitcnt vmcnt(14)
	v_add_f32_e32 v21, v21, v61
	s_waitcnt vmcnt(13)
	v_add_f32_e32 v21, v21, v62
	s_waitcnt vmcnt(12)
	v_add_f32_e32 v21, v21, v63
	s_waitcnt vmcnt(11)
	v_add_f32_e32 v21, v21, v64
	s_waitcnt vmcnt(10)
	v_add_f32_e32 v38, v21, v65
	s_waitcnt vmcnt(9)
	v_add_f32_e32 v19, v19, v66
	v_mov_b32_e32 v21, v43
	ds_read2st64_b32 v[40:41], v26 offset0:24 offset1:28
	ds_read2st64_b32 v[42:43], v26 offset0:16 offset1:20
	s_waitcnt vmcnt(8)
	v_add_f32_e32 v19, v19, v67
	s_waitcnt vmcnt(7)
	v_add_f32_e32 v44, v19, v68
	s_waitcnt vmcnt(6)
	v_pk_add_f32 v[20:21], v[44:45], v[20:21]
	s_waitcnt lgkmcnt(1)
	v_add_f32_e32 v37, v40, v41
	s_waitcnt vmcnt(5)
	v_pk_add_f32 v[20:21], v[20:21], v[32:33]
	s_waitcnt lgkmcnt(0)
	v_mov_b32_e32 v39, v42
	s_waitcnt vmcnt(3)
	v_pk_add_f32 v[20:21], v[20:21], v[28:29]
	v_mov_b32_e32 v35, v43
	v_fmamk_f32 v27, v20, 0x3a800000, v21
	s_waitcnt vmcnt(2)
	v_pk_add_f32 v[20:21], v[38:39], v[34:35]
	v_mov_b32_e32 v31, v29
	s_waitcnt vmcnt(1)
	v_pk_add_f32 v[20:21], v[20:21], v[36:37]
	v_ashrrev_i32_e32 v19, 31, v18
	s_waitcnt vmcnt(0)
	v_pk_add_f32 v[20:21], v[20:21], v[30:31]
	s_nop 0
	v_fmamk_f32 v28, v20, 0x39800000, v21
	v_lshl_add_u64 v[20:21], v[18:19], 2, s[14:15]
	global_store_dword v[20:21], v27, off
	ds_write_b32 v26, v28 offset:10240

	.amdhsa_kernel _Z14special_kernelPKtPKfS2_S2_S2_PfS3_S3_S2_S3_
		.amdhsa_group_segment_fixed_size 11264
		.amdhsa_private_segment_fixed_size 0
		.amdhsa_kernarg_size 80
		.amdhsa_user_sgpr_count 2
		.amdhsa_user_sgpr_dispatch_ptr 0
		.amdhsa_user_sgpr_queue_ptr 0
		.amdhsa_user_sgpr_kernarg_segment_ptr 1
		.amdhsa_user_sgpr_dispatch_id 0
		.amdhsa_user_sgpr_kernarg_preload_length 0
		.amdhsa_user_sgpr_kernarg_preload_offset 0
		.amdhsa_user_sgpr_private_segment_size 0
		.amdhsa_uses_dynamic_stack 0
		.amdhsa_enable_private_segment 0
		.amdhsa_system_sgpr_workgroup_id_x 1
		.amdhsa_system_sgpr_workgroup_id_y 0
		.amdhsa_system_sgpr_workgroup_id_z 0
		.amdhsa_system_sgpr_workgroup_info 0
		.amdhsa_system_vgpr_workitem_id 0
		.amdhsa_next_free_vgpr 128
		.amdhsa_next_free_sgpr 28
		.amdhsa_accum_offset 128
		.amdhsa_reserve_vcc 1
		.amdhsa_float_round_mode_32 0
		.amdhsa_float_round_mode_16_64 0
		.amdhsa_float_denorm_mode_32 3
		.amdhsa_float_denorm_mode_16_64 3
		.amdhsa_dx10_clamp 1
		.amdhsa_ieee_mode 1
		.amdhsa_fp16_overflow 0
		.amdhsa_tg_split 0
		.amdhsa_exception_fp_ieee_invalid_op 0
		.amdhsa_exception_fp_denorm_src 0
		.amdhsa_exception_fp_ieee_div_zero 0
		.amdhsa_exception_fp_ieee_overflow 0
		.amdhsa_exception_fp_ieee_underflow 0
		.amdhsa_exception_fp_ieee_inexact 0
		.amdhsa_exception_int_div_zero 0
	.end_amdhsa_kernel
